# speedup vs baseline: 1.0510x; 1.0006x over previous
_Z12scan_combinePKfPKDF16_S0_PDF16_:
	s_load_dwordx8 s[8:15], s[0:1], 0x0
	v_and_b32_e32 v1, 63, v0
	v_lshrrev_b32_e32 v90, 6, v0
	v_lshl_or_b32 v2, s2, 6, v1
	v_lshlrev_b32_e32 v3, 6, v2
	v_lshlrev_b32_e32 v2, 2, v2
	v_lshlrev_b32_e32 v88, 3, v0
	v_lshlrev_b32_e32 v89, 3, v1
	v_readfirstlane_b32 s5, v90
	s_lshl_b32 s6, s4, 6
	s_lshl_b32 s7, s5, 3
	s_add_i32 s6, s6, s7
	s_waitcnt lgkmcnt(0)
	s_lshl_b32 s7, s3, 3
	s_add_u32 s16, s8, s7
	s_addc_u32 s17, s9, 0
	global_load_dwordx2 v[4:5], v3, s[16:17]
	s_lshl_b32 s7, s6, 16
	s_lshl_b32 s18, s3, 13
	s_add_u32 s7, s7, s18
	s_add_u32 s20, s10, s7
	s_addc_u32 s21, s11, 0
	s_add_u32 s22, s14, s7
	s_addc_u32 s23, s15, 0
	s_lshl_b32 s7, s6, 13
	s_add_u32 s24, s12, s7
	s_addc_u32 s25, s13, 0
	global_load_dword v6, v2, s[20:21]
	s_add_u32 s20, s20, 0x10000
	s_addc_u32 s21, s21, 0
	global_load_dword v7, v2, s[20:21]
	s_add_u32 s20, s20, 0x10000
	s_addc_u32 s21, s21, 0
	global_load_dword v8, v2, s[20:21]
	s_add_u32 s20, s20, 0x10000
	s_addc_u32 s21, s21, 0
	global_load_dword v9, v2, s[20:21]
	s_add_u32 s20, s20, 0x10000
	s_addc_u32 s21, s21, 0
	global_load_dword v10, v2, s[20:21]
	s_add_u32 s20, s20, 0x10000
	s_addc_u32 s21, s21, 0
	global_load_dword v11, v2, s[20:21]
	s_add_u32 s20, s20, 0x10000
	s_addc_u32 s21, s21, 0
	global_load_dword v12, v2, s[20:21]
	s_add_u32 s20, s20, 0x10000
	s_addc_u32 s21, s21, 0
	global_load_dword v13, v2, s[20:21]
	global_load_dword v14, v2, s[24:25]
	s_add_u32 s24, s24, 0x2000
	s_addc_u32 s25, s25, 0
	global_load_dword v15, v2, s[24:25]
	s_add_u32 s24, s24, 0x2000
	s_addc_u32 s25, s25, 0
	global_load_dword v16, v2, s[24:25]
	s_add_u32 s24, s24, 0x2000
	s_addc_u32 s25, s25, 0
	global_load_dword v17, v2, s[24:25]
	s_add_u32 s24, s24, 0x2000
	s_addc_u32 s25, s25, 0
	global_load_dword v18, v2, s[24:25]
	s_add_u32 s24, s24, 0x2000
	s_addc_u32 s25, s25, 0
	global_load_dword v19, v2, s[24:25]
	s_add_u32 s24, s24, 0x2000
	s_addc_u32 s25, s25, 0
	global_load_dword v20, v2, s[24:25]
	s_add_u32 s24, s24, 0x2000
	s_addc_u32 s25, s25, 0
	global_load_dword v21, v2, s[24:25]
	s_waitcnt vmcnt(0)
	v_cvt_f32_f16_e32 v22, v6
	v_cvt_f32_f16_sdwa v23, v6 dst_sel:DWORD dst_unused:UNUSED_PAD src0_sel:WORD_1
	v_pk_mul_f32 v[52:53], v[14:15], v[4:5] op_sel_hi:[0,1]
	v_cvt_f32_f16_e32 v24, v7
	v_exp_f32_e32 v52, v52
	v_exp_f32_e32 v53, v53
	v_cvt_f32_f16_sdwa v25, v7 dst_sel:DWORD dst_unused:UNUSED_PAD src0_sel:WORD_1
	v_pk_mul_f32 v[54:55], v[14:15], v[4:5] op_sel:[1,0]
	v_cvt_f32_f16_e32 v26, v8
	v_exp_f32_e32 v54, v54
	v_exp_f32_e32 v55, v55
	v_cvt_f32_f16_sdwa v27, v8 dst_sel:DWORD dst_unused:UNUSED_PAD src0_sel:WORD_1
	v_pk_mul_f32 v[56:57], v[16:17], v[4:5] op_sel_hi:[0,1]
	v_cvt_f32_f16_e32 v28, v9
	v_exp_f32_e32 v56, v56
	v_exp_f32_e32 v57, v57
	v_cvt_f32_f16_sdwa v29, v9 dst_sel:DWORD dst_unused:UNUSED_PAD src0_sel:WORD_1
	v_pk_mul_f32 v[58:59], v[16:17], v[4:5] op_sel:[1,0]
	v_cvt_f32_f16_e32 v30, v10
	v_exp_f32_e32 v58, v58
	v_exp_f32_e32 v59, v59
	v_cvt_f32_f16_sdwa v31, v10 dst_sel:DWORD dst_unused:UNUSED_PAD src0_sel:WORD_1
	v_pk_mul_f32 v[60:61], v[18:19], v[4:5] op_sel_hi:[0,1]
	v_cvt_f32_f16_e32 v32, v11
	v_exp_f32_e32 v60, v60
	v_exp_f32_e32 v61, v61
	v_cvt_f32_f16_sdwa v33, v11 dst_sel:DWORD dst_unused:UNUSED_PAD src0_sel:WORD_1
	v_pk_mul_f32 v[62:63], v[18:19], v[4:5] op_sel:[1,0]
	v_cvt_f32_f16_e32 v34, v12
	v_exp_f32_e32 v62, v62
	v_exp_f32_e32 v63, v63
	v_cvt_f32_f16_sdwa v35, v12 dst_sel:DWORD dst_unused:UNUSED_PAD src0_sel:WORD_1
	v_pk_mul_f32 v[64:65], v[20:21], v[4:5] op_sel_hi:[0,1]
	v_cvt_f32_f16_e32 v36, v13
	v_exp_f32_e32 v64, v64
	v_exp_f32_e32 v65, v65
	v_cvt_f32_f16_sdwa v37, v13 dst_sel:DWORD dst_unused:UNUSED_PAD src0_sel:WORD_1
	v_pk_mul_f32 v[66:67], v[20:21], v[4:5] op_sel:[1,0]
	v_pk_fma_f32 v[38:39], v[54:55], v[22:23], v[24:25]
	v_exp_f32_e32 v66, v66
	v_exp_f32_e32 v67, v67
	v_pk_mul_f32 v[68:69], v[52:53], v[54:55]
	v_pk_fma_f32 v[40:41], v[56:57], v[38:39], v[26:27]
	v_pk_mul_f32 v[70:71], v[68:69], v[56:57]
	v_pk_fma_f32 v[42:43], v[58:59], v[40:41], v[28:29]
	v_pk_mul_f32 v[72:73], v[70:71], v[58:59]
	v_pk_fma_f32 v[44:45], v[60:61], v[42:43], v[30:31]
	v_pk_mul_f32 v[74:75], v[72:73], v[60:61]
	v_pk_fma_f32 v[46:47], v[62:63], v[44:45], v[32:33]
	v_pk_mul_f32 v[76:77], v[74:75], v[62:63]
	v_pk_fma_f32 v[48:49], v[64:65], v[46:47], v[34:35]
	v_pk_mul_f32 v[78:79], v[76:77], v[64:65]
	v_pk_fma_f32 v[50:51], v[66:67], v[48:49], v[36:37]
	v_pk_mul_f32 v[80:81], v[78:79], v[66:67]
	s_nop 0
	ds_write_b64 v88, v[80:81]
	ds_write_b64 v88, v[50:51] offset:4096
	v_mov_b32_e32 v82, 0
	v_mov_b32_e32 v83, 0
	s_waitcnt lgkmcnt(0)
	s_barrier
	ds_read_b64 v[92:93], v89
	ds_read_b64 v[106:107], v89 offset:4096
	ds_read_b64 v[94:95], v89 offset:512
	ds_read_b64 v[108:109], v89 offset:4608
	ds_read_b64 v[96:97], v89 offset:1024
	ds_read_b64 v[110:111], v89 offset:5120
	ds_read_b64 v[98:99], v89 offset:1536
	ds_read_b64 v[112:113], v89 offset:5632
	ds_read_b64 v[100:101], v89 offset:2048
	ds_read_b64 v[114:115], v89 offset:6144
	ds_read_b64 v[102:103], v89 offset:2560
	ds_read_b64 v[116:117], v89 offset:6656
	ds_read_b64 v[104:105], v89 offset:3072
	ds_read_b64 v[118:119], v89 offset:7168
	s_cmp_eq_u32 s5, 0
	s_cbranch_scc1 .Lcmb_out
	s_waitcnt lgkmcnt(0)
	v_mov_b32_e32 v82, v106
	v_mov_b32_e32 v83, v107
	s_cmp_le_u32 s5, 1
	s_cbranch_scc1 .Lcmb_out
	v_pk_fma_f32 v[82:83], v[94:95], v[82:83], v[108:109]
	s_cmp_le_u32 s5, 2
	s_cbranch_scc1 .Lcmb_out
	v_pk_fma_f32 v[82:83], v[96:97], v[82:83], v[110:111]
	s_cmp_le_u32 s5, 3
	s_cbranch_scc1 .Lcmb_out
	v_pk_fma_f32 v[82:83], v[98:99], v[82:83], v[112:113]
	s_cmp_le_u32 s5, 4
	s_cbranch_scc1 .Lcmb_out
	v_pk_fma_f32 v[82:83], v[100:101], v[82:83], v[114:115]
	s_cmp_le_u32 s5, 5
	s_cbranch_scc1 .Lcmb_out
	v_pk_fma_f32 v[82:83], v[102:103], v[82:83], v[116:117]
	s_cmp_le_u32 s5, 6
	s_cbranch_scc1 .Lcmb_out
	v_pk_fma_f32 v[82:83], v[104:105], v[82:83], v[118:119]
.Lcmb_out:
	s_waitcnt lgkmcnt(0)
	s_nop 0
	v_cvt_pk_f16_f32 v86, v82, v83
	global_store_dword v2, v86, s[22:23]
	s_add_u32 s22, s22, 0x10000
	s_addc_u32 s23, s23, 0
	v_pk_fma_f32 v[84:85], v[52:53], v[82:83], v[22:23]
	s_nop 0
	v_cvt_pk_f16_f32 v84, v84, v85
	global_store_dword v2, v84, s[22:23]
	s_add_u32 s22, s22, 0x10000
	s_addc_u32 s23, s23, 0
	v_pk_fma_f32 v[92:93], v[68:69], v[82:83], v[38:39]
	s_nop 0
	v_cvt_pk_f16_f32 v92, v92, v93
	global_store_dword v2, v92, s[22:23]
	s_add_u32 s22, s22, 0x10000
	s_addc_u32 s23, s23, 0
	v_pk_fma_f32 v[84:85], v[70:71], v[82:83], v[40:41]
	s_nop 0
	v_cvt_pk_f16_f32 v84, v84, v85
	global_store_dword v2, v84, s[22:23]
	s_add_u32 s22, s22, 0x10000
	s_addc_u32 s23, s23, 0
	v_pk_fma_f32 v[92:93], v[72:73], v[82:83], v[42:43]
	s_nop 0
	v_cvt_pk_f16_f32 v92, v92, v93
	global_store_dword v2, v92, s[22:23]
	s_add_u32 s22, s22, 0x10000
	s_addc_u32 s23, s23, 0
	v_pk_fma_f32 v[84:85], v[74:75], v[82:83], v[44:45]
	s_nop 0
	v_cvt_pk_f16_f32 v84, v84, v85
	global_store_dword v2, v84, s[22:23]
	s_add_u32 s22, s22, 0x10000
	s_addc_u32 s23, s23, 0
	v_pk_fma_f32 v[92:93], v[76:77], v[82:83], v[46:47]
	s_nop 0
	v_cvt_pk_f16_f32 v92, v92, v93
	global_store_dword v2, v92, s[22:23]
	s_add_u32 s22, s22, 0x10000
	s_addc_u32 s23, s23, 0
	v_pk_fma_f32 v[84:85], v[78:79], v[82:83], v[48:49]
	s_nop 0
	v_cvt_pk_f16_f32 v84, v84, v85
	global_store_dword v2, v84, s[22:23]
	s_endpgm
	.p2alignl 8, 3212836864

	.amdhsa_kernel _Z12scan_combinePKfPKDF16_S0_PDF16_
		.amdhsa_group_segment_fixed_size 8192
		.amdhsa_private_segment_fixed_size 0
		.amdhsa_kernarg_size 32
		.amdhsa_user_sgpr_count 2
		.amdhsa_user_sgpr_dispatch_ptr 0
		.amdhsa_user_sgpr_queue_ptr 0
		.amdhsa_user_sgpr_kernarg_segment_ptr 1
		.amdhsa_user_sgpr_dispatch_id 0
		.amdhsa_user_sgpr_kernarg_preload_length 0
		.amdhsa_user_sgpr_kernarg_preload_offset 0
		.amdhsa_user_sgpr_private_segment_size 0
		.amdhsa_uses_dynamic_stack 0
		.amdhsa_enable_private_segment 0
		.amdhsa_system_sgpr_workgroup_id_x 1
		.amdhsa_system_sgpr_workgroup_id_y 1
		.amdhsa_system_sgpr_workgroup_id_z 1
		.amdhsa_system_sgpr_workgroup_info 0
		.amdhsa_system_vgpr_workitem_id 0
		.amdhsa_next_free_vgpr 120
		.amdhsa_next_free_sgpr 26
		.amdhsa_accum_offset 120
		.amdhsa_reserve_vcc 1
		.amdhsa_float_round_mode_32 0
		.amdhsa_float_round_mode_16_64 0
		.amdhsa_float_denorm_mode_32 3
		.amdhsa_float_denorm_mode_16_64 3
		.amdhsa_dx10_clamp 1
		.amdhsa_ieee_mode 1
		.amdhsa_fp16_overflow 0
		.amdhsa_tg_split 0
		.amdhsa_exception_fp_ieee_invalid_op 0
		.amdhsa_exception_fp_denorm_src 0
		.amdhsa_exception_fp_ieee_div_zero 0
		.amdhsa_exception_fp_ieee_overflow 0
		.amdhsa_exception_fp_ieee_underflow 0
		.amdhsa_exception_fp_ieee_inexact 0
		.amdhsa_exception_int_div_zero 0
	.end_amdhsa_kernel

amdhsa.kernels:
  - .agpr_count:     0
    .args:
      - .address_space:  global
        .offset:         0
        .size:           8
        .value_kind:     global_buffer
      - .address_space:  global
        .offset:         8
        .size:           8
        .value_kind:     global_buffer
      - .offset:         16
        .size:           8
        .value_kind:     by_value
      - .address_space:  global
        .offset:         24
        .size:           8
        .value_kind:     global_buffer
      - .address_space:  global
        .offset:         32
        .size:           8
        .value_kind:     global_buffer
      - .offset:         40
        .size:           8
        .value_kind:     by_value
      - .address_space:  global
        .offset:         48
        .size:           8
        .value_kind:     global_buffer
      - .address_space:  global
        .offset:         56
        .size:           8
        .value_kind:     global_buffer
      - .offset:         64
        .size:           8
        .value_kind:     by_value
      - .address_space:  global
        .offset:         72
        .size:           8
        .value_kind:     global_buffer
      - .address_space:  global
        .offset:         80
        .size:           8
        .value_kind:     global_buffer
      - .offset:         88
        .size:           8
        .value_kind:     by_value
      - .address_space:  global
        .offset:         96
        .size:           8
        .value_kind:     global_buffer
      - .address_space:  global
        .offset:         104
        .size:           8
        .value_kind:     global_buffer
      - .offset:         112
        .size:           8
        .value_kind:     by_value
      - .address_space:  global
        .offset:         120
        .size:           8
        .value_kind:     global_buffer
      - .actual_access:  read_only
        .address_space:  global
        .offset:         128
        .size:           8
        .value_kind:     global_buffer
      - .actual_access:  write_only
        .address_space:  global
        .offset:         136
        .size:           8
        .value_kind:     global_buffer
    .group_segment_fixed_size: 0
    .kernarg_segment_align: 8
    .kernarg_segment_size: 144
    .language:       OpenCL C
    .language_version:
      - 2
      - 0
    .max_flat_workgroup_size: 256
    .name:           _Z10cvt_kernelPKfPDF16_lS0_S1_lS0_S1_lS0_S1_lS0_S1_lPjS0_Pf
    .private_segment_fixed_size: 0
    .sgpr_count:     58
    .sgpr_spill_count: 0
    .symbol:         _Z10cvt_kernelPKfPDF16_lS0_S1_lS0_S1_lS0_S1_lS0_S1_lPjS0_Pf.kd
    .uniform_work_group_size: 1
    .uses_dynamic_stack: false
    .vgpr_count:     18
    .vgpr_spill_count: 0
    .wavefront_size: 64
  - .agpr_count:     0
    .args:
      - .actual_access:  read_only
        .address_space:  global
        .offset:         0
        .size:           8
        .value_kind:     global_buffer
      - .actual_access:  read_only
        .address_space:  global
        .offset:         8
        .size:           8
        .value_kind:     global_buffer
      - .actual_access:  read_only
        .address_space:  global
        .offset:         16
        .size:           8
        .value_kind:     global_buffer
      - .actual_access:  read_only
        .address_space:  global
        .offset:         24
        .size:           8
        .value_kind:     global_buffer
      - .actual_access:  write_only
        .address_space:  global
        .offset:         32
        .size:           8
        .value_kind:     global_buffer
      - .actual_access:  write_only
        .address_space:  global
        .offset:         40
        .size:           8
        .value_kind:     global_buffer
      - .actual_access:  write_only
        .address_space:  global
        .offset:         48
        .size:           8
        .value_kind:     global_buffer
    .group_segment_fixed_size: 65792
    .kernarg_segment_align: 8
    .kernarg_segment_size: 56
    .language:       OpenCL C
    .language_version:
      - 2
      - 0
    .max_flat_workgroup_size: 1024
    .name:           _Z17conv_xproj_kernelPKDF16_PKfS2_S0_PDF16_S3_Pf
    .private_segment_fixed_size: 0
    .sgpr_count:     26
    .sgpr_spill_count: 0
    .symbol:         _Z17conv_xproj_kernelPKDF16_PKfS2_S0_PDF16_S3_Pf.kd
    .uniform_work_group_size: 1
    .uses_dynamic_stack: false
    .vgpr_count:     128
    .vgpr_spill_count: 0
    .wavefront_size: 64
  - .agpr_count:     0
    .args:
      - .actual_access:  read_only
        .address_space:  global
        .offset:         0
        .size:           8
        .value_kind:     global_buffer
      - .actual_access:  read_only
        .address_space:  global
        .offset:         8
        .size:           8
        .value_kind:     global_buffer
      - .actual_access:  read_only
        .address_space:  global
        .offset:         16
        .size:           8
        .value_kind:     global_buffer
      - .actual_access:  read_only
        .address_space:  global
        .offset:         24
        .size:           8
        .value_kind:     global_buffer
      - .actual_access:  read_only
        .address_space:  global
        .offset:         32
        .size:           8
        .value_kind:     global_buffer
      - .actual_access:  read_only
        .address_space:  global
        .offset:         40
        .size:           8
        .value_kind:     global_buffer
      - .actual_access:  write_only
        .address_space:  global
        .offset:         48
        .size:           8
        .value_kind:     global_buffer
      - .actual_access:  write_only
        .address_space:  global
        .offset:         56
        .size:           8
        .value_kind:     global_buffer
      - .actual_access:  write_only
        .address_space:  global
        .offset:         64
        .size:           8
        .value_kind:     global_buffer
      - .actual_access:  read_only
        .address_space:  global
        .offset:         72
        .size:           8
        .value_kind:     global_buffer
      - .actual_access:  write_only
        .address_space:  global
        .offset:         80
        .size:           8
        .value_kind:     global_buffer
    .group_segment_fixed_size: 4096
    .kernarg_segment_align: 8
    .kernarg_segment_size: 88
    .language:       OpenCL C
    .language_version:
      - 2
      - 0
    .max_flat_workgroup_size: 256
    .name:           _Z10scan_pass1PKDF16_S0_PKfS0_S2_S2_PDF16_PfS4_S2_S3_
    .private_segment_fixed_size: 0
    .sgpr_count:     94
    .sgpr_spill_count: 0
    .symbol:         _Z10scan_pass1PKDF16_S0_PKfS0_S2_S2_PDF16_PfS4_S2_S3_.kd
    .uniform_work_group_size: 1
    .uses_dynamic_stack: false
    .vgpr_count:     128
    .vgpr_spill_count: 0
    .wavefront_size: 64
  - .agpr_count:     0
    .args:
      - .actual_access:  read_only
        .address_space:  global
        .offset:         0
        .size:           8
        .value_kind:     global_buffer
      - .actual_access:  read_only
        .address_space:  global
        .offset:         8
        .size:           8
        .value_kind:     global_buffer
      - .actual_access:  read_only
        .address_space:  global
        .offset:         16
        .size:           8
        .value_kind:     global_buffer
      - .actual_access:  read_only
        .address_space:  global
        .offset:         24
        .size:           8
        .value_kind:     global_buffer
      - .actual_access:  read_only
        .address_space:  global
        .offset:         32
        .size:           8
        .value_kind:     global_buffer
      - .actual_access:  read_only
        .address_space:  global
        .offset:         40
        .size:           8
        .value_kind:     global_buffer
      - .actual_access:  write_only
        .address_space:  global
        .offset:         48
        .size:           8
        .value_kind:     global_buffer
      - .actual_access:  read_only
        .address_space:  global
        .offset:         56
        .size:           8
        .value_kind:     global_buffer
    .group_segment_fixed_size: 4096
    .kernarg_segment_align: 8
    .kernarg_segment_size: 64
    .language:       OpenCL C
    .language_version:
      - 2
      - 0
    .max_flat_workgroup_size: 256
    .name:           _Z10scan_pass2PKDF16_PKfS2_S0_S2_S0_PDF16_S2_
    .private_segment_fixed_size: 0
    .sgpr_count:     104
    .sgpr_spill_count: 0
    .symbol:         _Z10scan_pass2PKDF16_PKfS2_S0_S2_S0_PDF16_S2_.kd
    .uniform_work_group_size: 1
    .uses_dynamic_stack: false
    .vgpr_count:     118
    .vgpr_spill_count: 0
    .wavefront_size: 64
  - .agpr_count:     0
    .args:
      - .actual_access:  read_only
        .address_space:  global
        .offset:         0
        .size:           8
        .value_kind:     global_buffer
      - .actual_access:  read_only
        .address_space:  global
        .offset:         8
        .size:           8
        .value_kind:     global_buffer
      - .actual_access:  read_only
        .address_space:  global
        .offset:         16
        .size:           8
        .value_kind:     global_buffer
      - .actual_access:  write_only
        .address_space:  global
        .offset:         24
        .size:           8
        .value_kind:     global_buffer
    .group_segment_fixed_size: 8192
    .kernarg_segment_align: 8
    .kernarg_segment_size: 32
    .language:       OpenCL C
    .language_version:
      - 2
      - 0
    .max_flat_workgroup_size: 512
    .name:           _Z12scan_combinePKfPKDF16_S0_PDF16_
    .private_segment_fixed_size: 0
    .sgpr_count:     32
    .sgpr_spill_count: 0
    .symbol:         _Z12scan_combinePKfPKDF16_S0_PDF16_.kd
    .uniform_work_group_size: 1
    .uses_dynamic_stack: false
    .vgpr_count:     120
    .vgpr_spill_count: 0
    .wavefront_size: 64
  - .agpr_count:     0
    .args:
      - .address_space:  global
        .offset:         0
        .size:           8
        .value_kind:     global_buffer
      - .address_space:  global
        .offset:         8
        .size:           8
        .value_kind:     global_buffer
      - .actual_access:  write_only
        .address_space:  global
        .offset:         16
        .size:           8
        .value_kind:     global_buffer
      - .actual_access:  read_only
        .address_space:  global
        .offset:         24
        .size:           8
        .value_kind:     global_buffer
      - .offset:         32
        .size:           4
        .value_kind:     by_value
      - .actual_access:  read_only
        .address_space:  global
        .offset:         40
        .size:           8
        .value_kind:     global_buffer
    .group_segment_fixed_size: 0
    .kernarg_segment_align: 8
    .kernarg_segment_size: 48
    .language:       OpenCL C
    .language_version:
      - 2
      - 0
    .max_flat_workgroup_size: 512
    .name:           _Z11gemm_8phaseILi0ELi16ELi16ELi1024ELi1024ELi4096ELi1EEvPKDF16_S1_PvS2_fPj
    .private_segment_fixed_size: 0
    .sgpr_count:     38
    .sgpr_spill_count: 0
    .symbol:         _Z11gemm_8phaseILi0ELi16ELi16ELi1024ELi1024ELi4096ELi1EEvPKDF16_S1_PvS2_fPj.kd
    .uniform_work_group_size: 1
    .uses_dynamic_stack: false
    .vgpr_count:     236
    .vgpr_spill_count: 0
    .wavefront_size: 64
  - .agpr_count:     0
    .args:
      - .address_space:  global
        .offset:         0
        .size:           8
        .value_kind:     global_buffer
      - .address_space:  global
        .offset:         8
        .size:           8
        .value_kind:     global_buffer
      - .actual_access:  write_only
        .address_space:  global
        .offset:         16
        .size:           8
        .value_kind:     global_buffer
      - .address_space:  global
        .offset:         24
        .size:           8
        .value_kind:     global_buffer
      - .offset:         32
        .size:           4
        .value_kind:     by_value
      - .address_space:  global
        .offset:         40
        .size:           8
        .value_kind:     global_buffer
    .group_segment_fixed_size: 0
    .kernarg_segment_align: 8
    .kernarg_segment_size: 48
    .language:       OpenCL C
    .language_version:
      - 2
      - 0
    .max_flat_workgroup_size: 512
    .name:           _Z11gemm_8phaseILi1ELi16ELi4ELi512ELi2048ELi1024ELi4EEvPKDF16_S1_PvS2_fPj
    .private_segment_fixed_size: 0
    .sgpr_count:     41
    .sgpr_spill_count: 0
    .symbol:         _Z11gemm_8phaseILi1ELi16ELi4ELi512ELi2048ELi1024ELi4EEvPKDF16_S1_PvS2_fPj.kd
    .uniform_work_group_size: 1
    .uses_dynamic_stack: false
    .vgpr_count:     236
    .vgpr_spill_count: 0
    .wavefront_size: 64
  - .agpr_count:     0
    .args:
      - .address_space:  global
        .offset:         0
        .size:           8
        .value_kind:     global_buffer
      - .address_space:  global
        .offset:         8
        .size:           8
        .value_kind:     global_buffer
      - .actual_access:  write_only
        .address_space:  global
        .offset:         16
        .size:           8
        .value_kind:     global_buffer
      - .address_space:  global
        .offset:         24
        .size:           8
        .value_kind:     global_buffer
      - .offset:         32
        .size:           4
        .value_kind:     by_value
      - .address_space:  global
        .offset:         40
        .size:           8
        .value_kind:     global_buffer
    .group_segment_fixed_size: 0
    .kernarg_segment_align: 8
    .kernarg_segment_size: 48
    .language:       OpenCL C
    .language_version:
      - 2
      - 0
    .max_flat_workgroup_size: 512
    .name:           _Z11gemm_8phaseILi2ELi16ELi4ELi512ELi2048ELi1024ELi4EEvPKDF16_S1_PvS2_fPj
    .private_segment_fixed_size: 0
    .sgpr_count:     41
    .sgpr_spill_count: 0
    .symbol:         _Z11gemm_8phaseILi2ELi16ELi4ELi512ELi2048ELi1024ELi4EEvPKDF16_S1_PvS2_fPj.kd
    .uniform_work_group_size: 1
    .uses_dynamic_stack: false
    .vgpr_count:     236
    .vgpr_spill_count: 0
    .wavefront_size: 64
